# fp8 GEMM K-loops (in-proj e4m3, MoE gate/up, MoE down): leading wave half runs a loop copy with its counted DMA waits after each phase's MFMAs (on top of v34)
# baseline (speedup 1.0000x reference)
.LBB0_387:
	s_ashr_i32 s35, s34, 31
	ds_read_b128 v[18:21], v180
	ds_read_b128 v[22:25], v181
	ds_read_b128 v[26:29], v182
	ds_read_b128 v[30:33], v183
	ds_read_b128 v[2:5], v184
	ds_read_b128 v[6:9], v185
	ds_read_b128 v[10:13], v186
	ds_read_b128 v[14:17], v187
	s_lshl_b64 s[26:27], s[34:35], 18
	s_add_u32 s38, s53, s26
	s_addc_u32 s39, s54, s27
	s_and_b64 s[26:27], s[42:43], exec
	s_cselect_b32 s1, s39, s47
	s_cselect_b32 s5, s38, s46
	s_ashr_i32 s37, s36, 31
	s_lshl_b64 s[26:27], s[36:37], 18
	s_add_u32 s40, s55, s26
	s_addc_u32 s41, s56, s27
	s_and_b64 s[26:27], s[42:43], exec
	s_cselect_b32 s23, s41, s45
	s_cselect_b32 s26, s40, s44
	s_add_u32 s48, s46, 0x20080
	s_addc_u32 s49, s47, 0
	s_add_i32 s27, s57, 0xc000
	v_lshl_add_u64 v[224:225], s[48:49], 0, v[162:163]
	s_mov_b32 m0, s27
	s_add_i32 s35, s57, 0xe000
	ds_read_b128 v[172:175], v196
	ds_read_b128 v[176:179], v196 offset:1024
	ds_read_b128 v[198:201], v196 offset:2048
	ds_read_b128 v[202:205], v196 offset:3072
	ds_read_b128 v[206:209], v196 offset:4096
	ds_read_b128 v[210:213], v196 offset:5120
	ds_read_b128 v[216:219], v196 offset:6144
	ds_read_b128 v[220:223], v196 offset:7168
	global_load_lds_dwordx4 v[224:225], off
	v_lshl_add_u64 v[224:225], s[48:49], 0, v[164:165]
	s_mov_b32 m0, s35
	s_nop 0
	global_load_lds_dwordx4 v[224:225], off
	s_cmp_lg_u64 s[30:31], 0
	s_cbranch_scc1 .Lip8l_start
	s_cmp_eq_u32 s50, 1
	s_cbranch_scc1 .Lrw_first_ip8_0
	s_waitcnt vmcnt(24)
	s_branch .Lrw_done_ip8_0

.LBB0_388:
	ds_read_b128 v[2:5], v180
	ds_read_b128 v[6:9], v181
	ds_read_b128 v[10:13], v182
	ds_read_b128 v[14:17], v183
	ds_read_b128 v[26:29], v184
	ds_read_b128 v[30:33], v185
	ds_read_b128 v[172:175], v186
	ds_read_b128 v[176:179], v187
	s_add_u32 s44, s46, 0xfffe0080
	s_addc_u32 s45, s47, -1
	s_cmp_eq_u32 s75, 4
	s_cselect_b32 s49, s1, s45
	s_cselect_b32 s48, s5, s44
	s_cselect_b32 s45, s23, s74
	s_cselect_b32 s44, s26, s37
	s_mov_b32 m0, s27
	v_lshl_add_u64 v[224:225], s[46:47], 0, v[168:169]
	ds_read_b128 v[18:21], v196
	ds_read_b128 v[22:25], v196 offset:1024
	ds_read_b128 v[198:201], v196 offset:2048
	ds_read_b128 v[202:205], v196 offset:3072
	ds_read_b128 v[206:209], v196 offset:4096
	ds_read_b128 v[210:213], v196 offset:5120
	ds_read_b128 v[216:219], v196 offset:6144
	ds_read_b128 v[220:223], v196 offset:7168
	global_load_lds_dwordx4 v[224:225], off
	v_lshl_add_u64 v[224:225], s[46:47], 0, v[170:171]
	s_mov_b32 m0, s35
	s_nop 0
	global_load_lds_dwordx4 v[224:225], off
	s_waitcnt vmcnt(8)
	s_waitcnt lgkmcnt(0)
	s_barrier
	s_setprio 1
	s_waitcnt lgkmcnt(0)
	v_mfma_scale_f32_16x16x128_f8f6f4 v[158:161], v[2:9], v[18:25], v[158:161], v234, v235 op_sel_hi:[0,0,0]
	v_mfma_scale_f32_16x16x128_f8f6f4 v[154:157], v[10:17], v[18:25], v[154:157], v234, v235 op_sel_hi:[0,0,0]
	v_mfma_scale_f32_16x16x128_f8f6f4 v[150:153], v[2:9], v[198:205], v[150:153], v234, v235 op_sel_hi:[0,0,0]
	v_mfma_scale_f32_16x16x128_f8f6f4 v[146:149], v[10:17], v[198:205], v[146:149], v234, v235 op_sel_hi:[0,0,0]
	v_mfma_scale_f32_16x16x128_f8f6f4 v[142:145], v[2:9], v[206:213], v[142:145], v234, v235 op_sel_hi:[0,0,0]
	v_mfma_scale_f32_16x16x128_f8f6f4 v[138:141], v[10:17], v[206:213], v[138:141], v234, v235 op_sel_hi:[0,0,0]
	v_mfma_scale_f32_16x16x128_f8f6f4 v[134:137], v[2:9], v[216:223], v[134:137], v234, v235 op_sel_hi:[0,0,0]
	v_mfma_scale_f32_16x16x128_f8f6f4 v[130:133], v[10:17], v[216:223], v[130:133], v234, v235 op_sel_hi:[0,0,0]
	s_setprio 0
	s_setprio 1
	v_mfma_scale_f32_16x16x128_f8f6f4 v[126:129], v[26:33], v[18:25], v[126:129], v234, v235 op_sel_hi:[0,0,0]
	v_mfma_scale_f32_16x16x128_f8f6f4 v[122:125], v[172:179], v[18:25], v[122:125], v234, v235 op_sel_hi:[0,0,0]
	v_mfma_scale_f32_16x16x128_f8f6f4 v[118:121], v[26:33], v[198:205], v[118:121], v234, v235 op_sel_hi:[0,0,0]
	v_mfma_scale_f32_16x16x128_f8f6f4 v[114:117], v[172:179], v[198:205], v[114:117], v234, v235 op_sel_hi:[0,0,0]
	v_mfma_scale_f32_16x16x128_f8f6f4 v[110:113], v[26:33], v[206:213], v[110:113], v234, v235 op_sel_hi:[0,0,0]
	v_mfma_scale_f32_16x16x128_f8f6f4 v[106:109], v[172:179], v[206:213], v[106:109], v234, v235 op_sel_hi:[0,0,0]
	v_mfma_scale_f32_16x16x128_f8f6f4 v[102:105], v[26:33], v[216:223], v[102:105], v234, v235 op_sel_hi:[0,0,0]
	v_mfma_scale_f32_16x16x128_f8f6f4 v[98:101], v[172:179], v[216:223], v[98:101], v234, v235 op_sel_hi:[0,0,0]
	s_setprio 0
	s_barrier
	s_mov_b32 m0, s58
	v_lshl_add_u64 v[18:19], s[44:45], 0, v[0:1]
	s_add_u32 vcc_lo, s44, 0x20000
	ds_read_b128 v[198:201], v196 offset:16384
	ds_read_b128 v[202:205], v196 offset:17408
	ds_read_b128 v[206:209], v196 offset:18432
	ds_read_b128 v[210:213], v196 offset:19456
	ds_read_b128 v[216:219], v196 offset:20480
	ds_read_b128 v[220:223], v196 offset:21504
	ds_read_b128 v[224:227], v196 offset:22528
	ds_read_b128 v[228:231], v196 offset:23552
	global_load_lds_dwordx4 v[18:19], off
	v_lshl_add_u64 v[20:21], s[44:45], 0, v[166:167]
	s_mov_b32 m0, s59
	s_addc_u32 vcc_hi, s45, 0
	global_load_lds_dwordx4 v[20:21], off
	v_lshl_add_u64 v[22:23], vcc, 0, v[0:1]
	s_mov_b32 m0, s60
	v_lshl_add_u64 v[24:25], s[48:49], 0, v[164:165]
	global_load_lds_dwordx4 v[22:23], off
	v_lshl_add_u64 v[22:23], vcc, 0, v[166:167]
	s_mov_b32 m0, s61
	s_nop 0
	global_load_lds_dwordx4 v[22:23], off
	v_lshl_add_u64 v[22:23], s[48:49], 0, v[162:163]
	s_mov_b32 m0, s57
	s_nop 0
	global_load_lds_dwordx4 v[22:23], off
	s_mov_b32 m0, s62
	s_nop 0
	global_load_lds_dwordx4 v[24:25], off
	s_waitcnt vmcnt(8)
	s_waitcnt lgkmcnt(0)
	s_barrier
	s_setprio 1
	s_waitcnt lgkmcnt(0)
	v_mfma_scale_f32_16x16x128_f8f6f4 v[94:97], v[2:9], v[198:205], v[94:97], v234, v235 op_sel_hi:[0,0,0]
	v_mfma_scale_f32_16x16x128_f8f6f4 v[90:93], v[10:17], v[198:205], v[90:93], v234, v235 op_sel_hi:[0,0,0]
	v_mfma_scale_f32_16x16x128_f8f6f4 v[86:89], v[2:9], v[206:213], v[86:89], v234, v235 op_sel_hi:[0,0,0]
	v_mfma_scale_f32_16x16x128_f8f6f4 v[82:85], v[10:17], v[206:213], v[82:85], v234, v235 op_sel_hi:[0,0,0]
	v_mfma_scale_f32_16x16x128_f8f6f4 v[78:81], v[2:9], v[216:223], v[78:81], v234, v235 op_sel_hi:[0,0,0]
	v_mfma_scale_f32_16x16x128_f8f6f4 v[74:77], v[10:17], v[216:223], v[74:77], v234, v235 op_sel_hi:[0,0,0]
	v_mfma_scale_f32_16x16x128_f8f6f4 v[70:73], v[2:9], v[224:231], v[70:73], v234, v235 op_sel_hi:[0,0,0]
	v_mfma_scale_f32_16x16x128_f8f6f4 v[66:69], v[10:17], v[224:231], v[66:69], v234, v235 op_sel_hi:[0,0,0]
	s_setprio 0
	s_setprio 1
	v_mfma_scale_f32_16x16x128_f8f6f4 v[62:65], v[26:33], v[198:205], v[62:65], v234, v235 op_sel_hi:[0,0,0]
	v_mfma_scale_f32_16x16x128_f8f6f4 v[58:61], v[172:179], v[198:205], v[58:61], v234, v235 op_sel_hi:[0,0,0]
	v_mfma_scale_f32_16x16x128_f8f6f4 v[54:57], v[26:33], v[206:213], v[54:57], v234, v235 op_sel_hi:[0,0,0]
	v_mfma_scale_f32_16x16x128_f8f6f4 v[50:53], v[172:179], v[206:213], v[50:53], v234, v235 op_sel_hi:[0,0,0]
	v_mfma_scale_f32_16x16x128_f8f6f4 v[46:49], v[26:33], v[216:223], v[46:49], v234, v235 op_sel_hi:[0,0,0]
	v_mfma_scale_f32_16x16x128_f8f6f4 v[42:45], v[172:179], v[216:223], v[42:45], v234, v235 op_sel_hi:[0,0,0]
	v_mfma_scale_f32_16x16x128_f8f6f4 v[38:41], v[26:33], v[224:231], v[38:41], v234, v235 op_sel_hi:[0,0,0]
	v_mfma_scale_f32_16x16x128_f8f6f4 v[34:37], v[172:179], v[224:231], v[34:37], v234, v235 op_sel_hi:[0,0,0]
	s_setprio 0
	s_barrier
	ds_read_b128 v[10:13], v188
	ds_read_b128 v[14:17], v189
	ds_read_b128 v[26:29], v190
	ds_read_b128 v[30:33], v191
	ds_read_b128 v[2:5], v192
	ds_read_b128 v[6:9], v193
	ds_read_b128 v[172:175], v194
	ds_read_b128 v[176:179], v195
	s_add_u32 s48, s48, 0x20000
	s_addc_u32 s49, s49, 0
	s_mov_b32 m0, s63
	v_lshl_add_u64 v[232:233], s[48:49], 0, v[162:163]
	ds_read_b128 v[198:201], v196 offset:32768
	ds_read_b128 v[202:205], v196 offset:33792
	ds_read_b128 v[206:209], v196 offset:34816
	ds_read_b128 v[210:213], v196 offset:35840
	ds_read_b128 v[216:219], v196 offset:36864
	ds_read_b128 v[220:223], v196 offset:37888
	ds_read_b128 v[224:227], v196 offset:38912
	ds_read_b128 v[228:231], v196 offset:39936
	global_load_lds_dwordx4 v[232:233], off
	v_lshl_add_u64 v[232:233], s[48:49], 0, v[164:165]
	s_mov_b32 m0, s64
	s_nop 0
	global_load_lds_dwordx4 v[232:233], off
	s_waitcnt vmcnt(8)
	s_waitcnt lgkmcnt(0)
	s_barrier
	s_setprio 1
	s_waitcnt lgkmcnt(0)
	v_mfma_scale_f32_16x16x128_f8f6f4 v[158:161], v[10:17], v[198:205], v[158:161], v234, v235 op_sel_hi:[0,0,0]
	v_mfma_scale_f32_16x16x128_f8f6f4 v[154:157], v[26:33], v[198:205], v[154:157], v234, v235 op_sel_hi:[0,0,0]
	v_mfma_scale_f32_16x16x128_f8f6f4 v[150:153], v[10:17], v[206:213], v[150:153], v234, v235 op_sel_hi:[0,0,0]
	v_mfma_scale_f32_16x16x128_f8f6f4 v[146:149], v[26:33], v[206:213], v[146:149], v234, v235 op_sel_hi:[0,0,0]
	v_mfma_scale_f32_16x16x128_f8f6f4 v[142:145], v[10:17], v[216:223], v[142:145], v234, v235 op_sel_hi:[0,0,0]
	v_mfma_scale_f32_16x16x128_f8f6f4 v[138:141], v[26:33], v[216:223], v[138:141], v234, v235 op_sel_hi:[0,0,0]
	v_mfma_scale_f32_16x16x128_f8f6f4 v[134:137], v[10:17], v[224:231], v[134:137], v234, v235 op_sel_hi:[0,0,0]
	v_mfma_scale_f32_16x16x128_f8f6f4 v[130:133], v[26:33], v[224:231], v[130:133], v234, v235 op_sel_hi:[0,0,0]
	s_setprio 0
	s_setprio 1
	v_mfma_scale_f32_16x16x128_f8f6f4 v[126:129], v[2:9], v[198:205], v[126:129], v234, v235 op_sel_hi:[0,0,0]
	v_mfma_scale_f32_16x16x128_f8f6f4 v[122:125], v[172:179], v[198:205], v[122:125], v234, v235 op_sel_hi:[0,0,0]
	v_mfma_scale_f32_16x16x128_f8f6f4 v[118:121], v[2:9], v[206:213], v[118:121], v234, v235 op_sel_hi:[0,0,0]
	v_mfma_scale_f32_16x16x128_f8f6f4 v[114:117], v[172:179], v[206:213], v[114:117], v234, v235 op_sel_hi:[0,0,0]
	v_mfma_scale_f32_16x16x128_f8f6f4 v[110:113], v[2:9], v[216:223], v[110:113], v234, v235 op_sel_hi:[0,0,0]
	v_mfma_scale_f32_16x16x128_f8f6f4 v[106:109], v[172:179], v[216:223], v[106:109], v234, v235 op_sel_hi:[0,0,0]
	v_mfma_scale_f32_16x16x128_f8f6f4 v[102:105], v[2:9], v[224:231], v[102:105], v234, v235 op_sel_hi:[0,0,0]
	v_mfma_scale_f32_16x16x128_f8f6f4 v[98:101], v[172:179], v[224:231], v[98:101], v234, v235 op_sel_hi:[0,0,0]
	s_setprio 0
	s_barrier
	s_mov_b32 m0, s7
	v_lshl_add_u64 v[18:19], v[18:19], 0, s[66:67]
	s_add_u32 s44, s44, 0x20080
	ds_read_b128 v[198:201], v196 offset:49152
	ds_read_b128 v[202:205], v196 offset:50176
	ds_read_b128 v[206:209], v196 offset:51200
	ds_read_b128 v[210:213], v196 offset:52224
	ds_read_b128 v[216:219], v196 offset:53248
	ds_read_b128 v[220:223], v196 offset:54272
	ds_read_b128 v[224:227], v196 offset:55296
	ds_read_b128 v[228:231], v196 offset:56320
	global_load_lds_dwordx4 v[18:19], off
	v_lshl_add_u64 v[18:19], v[20:21], 0, s[66:67]
	s_mov_b32 m0, s65
	s_addc_u32 s45, s45, 0
	global_load_lds_dwordx4 v[18:19], off
	v_lshl_add_u64 v[18:19], s[44:45], 0, v[0:1]
	s_mov_b32 m0, s13
	s_nop 0
	global_load_lds_dwordx4 v[18:19], off
	v_lshl_add_u64 v[18:19], s[44:45], 0, v[166:167]
	s_mov_b32 m0, s51
	s_nop 0
	global_load_lds_dwordx4 v[18:19], off
	v_lshl_add_u64 v[18:19], v[22:23], 0, s[66:67]
	s_mov_b32 m0, s68
	s_nop 0
	global_load_lds_dwordx4 v[18:19], off
	v_lshl_add_u64 v[18:19], v[24:25], 0, s[66:67]
	s_mov_b32 m0, s52
	s_nop 0
	global_load_lds_dwordx4 v[18:19], off
	s_waitcnt vmcnt(8)
	s_waitcnt lgkmcnt(0)
	s_barrier
	s_setprio 1
	s_waitcnt lgkmcnt(0)
	v_mfma_scale_f32_16x16x128_f8f6f4 v[94:97], v[10:17], v[198:205], v[94:97], v234, v235 op_sel_hi:[0,0,0]
	v_mfma_scale_f32_16x16x128_f8f6f4 v[90:93], v[26:33], v[198:205], v[90:93], v234, v235 op_sel_hi:[0,0,0]
	v_mfma_scale_f32_16x16x128_f8f6f4 v[86:89], v[10:17], v[206:213], v[86:89], v234, v235 op_sel_hi:[0,0,0]
	v_mfma_scale_f32_16x16x128_f8f6f4 v[82:85], v[26:33], v[206:213], v[82:85], v234, v235 op_sel_hi:[0,0,0]
	v_mfma_scale_f32_16x16x128_f8f6f4 v[78:81], v[10:17], v[216:223], v[78:81], v234, v235 op_sel_hi:[0,0,0]
	v_mfma_scale_f32_16x16x128_f8f6f4 v[74:77], v[26:33], v[216:223], v[74:77], v234, v235 op_sel_hi:[0,0,0]
	v_mfma_scale_f32_16x16x128_f8f6f4 v[70:73], v[10:17], v[224:231], v[70:73], v234, v235 op_sel_hi:[0,0,0]
	v_mfma_scale_f32_16x16x128_f8f6f4 v[66:69], v[26:33], v[224:231], v[66:69], v234, v235 op_sel_hi:[0,0,0]
	s_setprio 0
	s_setprio 1
	v_mfma_scale_f32_16x16x128_f8f6f4 v[62:65], v[2:9], v[198:205], v[62:65], v234, v235 op_sel_hi:[0,0,0]
	v_mfma_scale_f32_16x16x128_f8f6f4 v[58:61], v[172:179], v[198:205], v[58:61], v234, v235 op_sel_hi:[0,0,0]
	v_mfma_scale_f32_16x16x128_f8f6f4 v[54:57], v[2:9], v[206:213], v[54:57], v234, v235 op_sel_hi:[0,0,0]
	v_mfma_scale_f32_16x16x128_f8f6f4 v[50:53], v[172:179], v[206:213], v[50:53], v234, v235 op_sel_hi:[0,0,0]
	v_mfma_scale_f32_16x16x128_f8f6f4 v[46:49], v[2:9], v[216:223], v[46:49], v234, v235 op_sel_hi:[0,0,0]
	v_mfma_scale_f32_16x16x128_f8f6f4 v[42:45], v[172:179], v[216:223], v[42:45], v234, v235 op_sel_hi:[0,0,0]
	v_mfma_scale_f32_16x16x128_f8f6f4 v[38:41], v[2:9], v[224:231], v[38:41], v234, v235 op_sel_hi:[0,0,0]
	v_mfma_scale_f32_16x16x128_f8f6f4 v[34:37], v[172:179], v[224:231], v[34:37], v234, v235 op_sel_hi:[0,0,0]
	s_setprio 0
	s_barrier
	s_add_i32 s75, s75, 2
	s_add_u32 s46, s46, 0x100
	s_addc_u32 s47, s47, 0
	s_add_u32 s37, s37, 0x100
	s_addc_u32 s74, s74, 0
	s_cmp_gt_u32 s75, 5
	s_cbranch_scc0 .LBB0_388
	s_branch .Lip8_join
.Lip8l_start:
	s_waitcnt lgkmcnt(0)
	s_barrier
	s_setprio 1
	s_waitcnt lgkmcnt(0)
	v_mfma_scale_f32_16x16x128_f8f6f4 v[158:161], v[18:25], v[172:179], 0, v234, v235 op_sel_hi:[0,0,0]
	v_mfma_scale_f32_16x16x128_f8f6f4 v[154:157], v[26:33], v[172:179], 0, v234, v235 op_sel_hi:[0,0,0]
	v_mfma_scale_f32_16x16x128_f8f6f4 v[150:153], v[18:25], v[198:205], 0, v234, v235 op_sel_hi:[0,0,0]
	v_mfma_scale_f32_16x16x128_f8f6f4 v[146:149], v[26:33], v[198:205], 0, v234, v235 op_sel_hi:[0,0,0]
	v_mfma_scale_f32_16x16x128_f8f6f4 v[142:145], v[18:25], v[206:213], 0, v234, v235 op_sel_hi:[0,0,0]
	v_mfma_scale_f32_16x16x128_f8f6f4 v[138:141], v[26:33], v[206:213], 0, v234, v235 op_sel_hi:[0,0,0]
	v_mfma_scale_f32_16x16x128_f8f6f4 v[134:137], v[18:25], v[216:223], 0, v234, v235 op_sel_hi:[0,0,0]
	v_mfma_scale_f32_16x16x128_f8f6f4 v[130:133], v[26:33], v[216:223], 0, v234, v235 op_sel_hi:[0,0,0]
	s_setprio 0
	s_setprio 1
	v_mfma_scale_f32_16x16x128_f8f6f4 v[126:129], v[2:9], v[172:179], 0, v234, v235 op_sel_hi:[0,0,0]
	v_mfma_scale_f32_16x16x128_f8f6f4 v[122:125], v[10:17], v[172:179], 0, v234, v235 op_sel_hi:[0,0,0]
	v_mfma_scale_f32_16x16x128_f8f6f4 v[118:121], v[2:9], v[198:205], 0, v234, v235 op_sel_hi:[0,0,0]
	v_mfma_scale_f32_16x16x128_f8f6f4 v[114:117], v[10:17], v[198:205], 0, v234, v235 op_sel_hi:[0,0,0]
	v_mfma_scale_f32_16x16x128_f8f6f4 v[110:113], v[2:9], v[206:213], 0, v234, v235 op_sel_hi:[0,0,0]
	v_mfma_scale_f32_16x16x128_f8f6f4 v[106:109], v[10:17], v[206:213], 0, v234, v235 op_sel_hi:[0,0,0]
	v_mfma_scale_f32_16x16x128_f8f6f4 v[102:105], v[2:9], v[216:223], 0, v234, v235 op_sel_hi:[0,0,0]
	v_mfma_scale_f32_16x16x128_f8f6f4 v[98:101], v[10:17], v[216:223], 0, v234, v235 op_sel_hi:[0,0,0]
	s_setprio 0
	s_cmp_eq_u32 s50, 1
	s_cbranch_scc1 .Lip8l_rw_first_ip8_0
	s_waitcnt vmcnt(24)
	s_branch .Lip8l_rw_done_ip8_0

.Lip8l_rw_done_ip8_0:
	s_barrier
	v_lshl_add_u64 v[172:173], s[44:45], 0, v[0:1]
	s_mov_b64 s[74:75], 0x100
	s_mov_b32 m0, s58
	v_lshl_add_u64 v[174:175], v[172:173], 0, s[74:75]
	ds_read_b128 v[198:201], v196 offset:16384
	ds_read_b128 v[202:205], v196 offset:17408
	ds_read_b128 v[206:209], v196 offset:18432
	ds_read_b128 v[210:213], v196 offset:19456
	ds_read_b128 v[216:219], v196 offset:20480
	ds_read_b128 v[220:223], v196 offset:21504
	ds_read_b128 v[224:227], v196 offset:22528
	ds_read_b128 v[228:231], v196 offset:23552
	global_load_lds_dwordx4 v[174:175], off
	v_lshl_add_u64 v[174:175], s[44:45], 0, v[166:167]
	s_add_u32 s48, s44, 0x20100
	v_lshl_add_u64 v[176:177], v[174:175], 0, s[74:75]
	s_mov_b32 m0, s59
	s_addc_u32 s49, s45, 0
	global_load_lds_dwordx4 v[176:177], off
	v_lshl_add_u64 v[176:177], s[48:49], 0, v[0:1]
	s_mov_b32 m0, s60
	s_nop 0
	global_load_lds_dwordx4 v[176:177], off
	v_lshl_add_u64 v[176:177], s[48:49], 0, v[166:167]
	s_mov_b32 m0, s61
	s_nop 0
	global_load_lds_dwordx4 v[176:177], off
	v_lshl_add_u64 v[176:177], s[46:47], 0, v[162:163]
	v_lshl_add_u64 v[178:179], v[176:177], 0, s[74:75]
	s_mov_b32 m0, s57
	s_nop 0
	global_load_lds_dwordx4 v[178:179], off
	v_lshl_add_u64 v[178:179], s[46:47], 0, v[164:165]
	v_lshl_add_u64 v[232:233], v[178:179], 0, s[74:75]
	s_mov_b32 m0, s62
	s_nop 0
	global_load_lds_dwordx4 v[232:233], off
	s_waitcnt lgkmcnt(0)
	s_barrier
	s_setprio 1
	s_waitcnt lgkmcnt(0)
	v_mfma_scale_f32_16x16x128_f8f6f4 v[94:97], v[18:25], v[198:205], 0, v234, v235 op_sel_hi:[0,0,0]
	v_mfma_scale_f32_16x16x128_f8f6f4 v[90:93], v[26:33], v[198:205], 0, v234, v235 op_sel_hi:[0,0,0]
	v_mfma_scale_f32_16x16x128_f8f6f4 v[86:89], v[18:25], v[206:213], 0, v234, v235 op_sel_hi:[0,0,0]
	v_mfma_scale_f32_16x16x128_f8f6f4 v[82:85], v[26:33], v[206:213], 0, v234, v235 op_sel_hi:[0,0,0]
	v_mfma_scale_f32_16x16x128_f8f6f4 v[78:81], v[18:25], v[216:223], 0, v234, v235 op_sel_hi:[0,0,0]
	v_mfma_scale_f32_16x16x128_f8f6f4 v[74:77], v[26:33], v[216:223], 0, v234, v235 op_sel_hi:[0,0,0]
	v_mfma_scale_f32_16x16x128_f8f6f4 v[70:73], v[18:25], v[224:231], 0, v234, v235 op_sel_hi:[0,0,0]
	v_mfma_scale_f32_16x16x128_f8f6f4 v[66:69], v[26:33], v[224:231], 0, v234, v235 op_sel_hi:[0,0,0]
	s_setprio 0
	s_setprio 1
	v_mfma_scale_f32_16x16x128_f8f6f4 v[62:65], v[2:9], v[198:205], 0, v234, v235 op_sel_hi:[0,0,0]
	v_mfma_scale_f32_16x16x128_f8f6f4 v[58:61], v[10:17], v[198:205], 0, v234, v235 op_sel_hi:[0,0,0]
	v_mfma_scale_f32_16x16x128_f8f6f4 v[54:57], v[2:9], v[206:213], 0, v234, v235 op_sel_hi:[0,0,0]
	v_mfma_scale_f32_16x16x128_f8f6f4 v[50:53], v[10:17], v[206:213], 0, v234, v235 op_sel_hi:[0,0,0]
	v_mfma_scale_f32_16x16x128_f8f6f4 v[46:49], v[2:9], v[216:223], 0, v234, v235 op_sel_hi:[0,0,0]
	v_mfma_scale_f32_16x16x128_f8f6f4 v[42:45], v[10:17], v[216:223], 0, v234, v235 op_sel_hi:[0,0,0]
	v_mfma_scale_f32_16x16x128_f8f6f4 v[38:41], v[2:9], v[224:231], 0, v234, v235 op_sel_hi:[0,0,0]
	v_mfma_scale_f32_16x16x128_f8f6f4 v[34:37], v[10:17], v[224:231], 0, v234, v235 op_sel_hi:[0,0,0]
	s_setprio 0
	s_cmp_eq_u32 s50, 1
	s_cbranch_scc1 .Lip8l_rw_first_ip8_1
	s_waitcnt vmcnt(24)
	s_branch .Lip8l_rw_done_ip8_1

.Lip8l_rw_done_ip8_1:
	s_barrier
	ds_read_b128 v[18:21], v188
	ds_read_b128 v[22:25], v189
	ds_read_b128 v[26:29], v190
	ds_read_b128 v[30:33], v191
	ds_read_b128 v[2:5], v192
	ds_read_b128 v[6:9], v193
	ds_read_b128 v[10:13], v194
	ds_read_b128 v[14:17], v195
	s_add_u32 s48, s46, 0x20100
	s_addc_u32 s49, s47, 0
	s_mov_b32 m0, s63
	v_lshl_add_u64 v[232:233], s[48:49], 0, v[162:163]
	ds_read_b128 v[198:201], v196 offset:32768
	ds_read_b128 v[202:205], v196 offset:33792
	ds_read_b128 v[206:209], v196 offset:34816
	ds_read_b128 v[210:213], v196 offset:35840
	ds_read_b128 v[216:219], v196 offset:36864
	ds_read_b128 v[220:223], v196 offset:37888
	ds_read_b128 v[224:227], v196 offset:38912
	ds_read_b128 v[228:231], v196 offset:39936
	global_load_lds_dwordx4 v[232:233], off
	v_lshl_add_u64 v[232:233], s[48:49], 0, v[164:165]
	s_mov_b32 m0, s64
	s_nop 0
	global_load_lds_dwordx4 v[232:233], off
	s_waitcnt lgkmcnt(0)
	s_barrier
	s_setprio 1
	s_waitcnt lgkmcnt(0)
	v_mfma_scale_f32_16x16x128_f8f6f4 v[158:161], v[18:25], v[198:205], v[158:161], v234, v235 op_sel_hi:[0,0,0]
	v_mfma_scale_f32_16x16x128_f8f6f4 v[154:157], v[26:33], v[198:205], v[154:157], v234, v235 op_sel_hi:[0,0,0]
	v_mfma_scale_f32_16x16x128_f8f6f4 v[150:153], v[18:25], v[206:213], v[150:153], v234, v235 op_sel_hi:[0,0,0]
	v_mfma_scale_f32_16x16x128_f8f6f4 v[146:149], v[26:33], v[206:213], v[146:149], v234, v235 op_sel_hi:[0,0,0]
	v_mfma_scale_f32_16x16x128_f8f6f4 v[142:145], v[18:25], v[216:223], v[142:145], v234, v235 op_sel_hi:[0,0,0]
	v_mfma_scale_f32_16x16x128_f8f6f4 v[138:141], v[26:33], v[216:223], v[138:141], v234, v235 op_sel_hi:[0,0,0]
	v_mfma_scale_f32_16x16x128_f8f6f4 v[134:137], v[18:25], v[224:231], v[134:137], v234, v235 op_sel_hi:[0,0,0]
	v_mfma_scale_f32_16x16x128_f8f6f4 v[130:133], v[26:33], v[224:231], v[130:133], v234, v235 op_sel_hi:[0,0,0]
	s_setprio 0
	s_setprio 1
	v_mfma_scale_f32_16x16x128_f8f6f4 v[126:129], v[2:9], v[198:205], v[126:129], v234, v235 op_sel_hi:[0,0,0]
	v_mfma_scale_f32_16x16x128_f8f6f4 v[122:125], v[10:17], v[198:205], v[122:125], v234, v235 op_sel_hi:[0,0,0]
	v_mfma_scale_f32_16x16x128_f8f6f4 v[118:121], v[2:9], v[206:213], v[118:121], v234, v235 op_sel_hi:[0,0,0]
	v_mfma_scale_f32_16x16x128_f8f6f4 v[114:117], v[10:17], v[206:213], v[114:117], v234, v235 op_sel_hi:[0,0,0]
	v_mfma_scale_f32_16x16x128_f8f6f4 v[110:113], v[2:9], v[216:223], v[110:113], v234, v235 op_sel_hi:[0,0,0]
	v_mfma_scale_f32_16x16x128_f8f6f4 v[106:109], v[10:17], v[216:223], v[106:109], v234, v235 op_sel_hi:[0,0,0]
	v_mfma_scale_f32_16x16x128_f8f6f4 v[102:105], v[2:9], v[224:231], v[102:105], v234, v235 op_sel_hi:[0,0,0]
	v_mfma_scale_f32_16x16x128_f8f6f4 v[98:101], v[10:17], v[224:231], v[98:101], v234, v235 op_sel_hi:[0,0,0]
	s_setprio 0
	s_waitcnt vmcnt(8)
	s_barrier
	s_mov_b64 s[74:75], 0x180
	s_mov_b32 m0, s7
	v_lshl_add_u64 v[172:173], v[172:173], 0, s[74:75]
	s_add_u32 s48, s44, 0x20180
	ds_read_b128 v[198:201], v196 offset:49152
	ds_read_b128 v[202:205], v196 offset:50176
	ds_read_b128 v[206:209], v196 offset:51200
	ds_read_b128 v[210:213], v196 offset:52224
	ds_read_b128 v[216:219], v196 offset:53248
	ds_read_b128 v[220:223], v196 offset:54272
	ds_read_b128 v[224:227], v196 offset:55296
	ds_read_b128 v[228:231], v196 offset:56320
	global_load_lds_dwordx4 v[172:173], off
	v_lshl_add_u64 v[172:173], v[174:175], 0, s[74:75]
	s_mov_b32 m0, s65
	s_addc_u32 s49, s45, 0
	global_load_lds_dwordx4 v[172:173], off
	v_lshl_add_u64 v[172:173], s[48:49], 0, v[0:1]
	s_mov_b32 m0, s13
	s_nop 0
	global_load_lds_dwordx4 v[172:173], off
	v_lshl_add_u64 v[172:173], s[48:49], 0, v[166:167]
	s_mov_b32 m0, s51
	s_nop 0
	global_load_lds_dwordx4 v[172:173], off
	v_lshl_add_u64 v[172:173], v[176:177], 0, s[74:75]
	s_mov_b32 m0, s68
	s_nop 0
	global_load_lds_dwordx4 v[172:173], off
	v_lshl_add_u64 v[172:173], v[178:179], 0, s[74:75]
	s_mov_b32 m0, s52
	s_nop 0
	global_load_lds_dwordx4 v[172:173], off
	s_waitcnt lgkmcnt(0)
	s_barrier
	s_setprio 1
	s_waitcnt lgkmcnt(0)
	v_mfma_scale_f32_16x16x128_f8f6f4 v[94:97], v[18:25], v[198:205], v[94:97], v234, v235 op_sel_hi:[0,0,0]
	v_mfma_scale_f32_16x16x128_f8f6f4 v[90:93], v[26:33], v[198:205], v[90:93], v234, v235 op_sel_hi:[0,0,0]
	v_mfma_scale_f32_16x16x128_f8f6f4 v[86:89], v[18:25], v[206:213], v[86:89], v234, v235 op_sel_hi:[0,0,0]
	v_mfma_scale_f32_16x16x128_f8f6f4 v[82:85], v[26:33], v[206:213], v[82:85], v234, v235 op_sel_hi:[0,0,0]
	v_mfma_scale_f32_16x16x128_f8f6f4 v[78:81], v[18:25], v[216:223], v[78:81], v234, v235 op_sel_hi:[0,0,0]
	v_mfma_scale_f32_16x16x128_f8f6f4 v[74:77], v[26:33], v[216:223], v[74:77], v234, v235 op_sel_hi:[0,0,0]
	v_mfma_scale_f32_16x16x128_f8f6f4 v[70:73], v[18:25], v[224:231], v[70:73], v234, v235 op_sel_hi:[0,0,0]
	v_mfma_scale_f32_16x16x128_f8f6f4 v[66:69], v[26:33], v[224:231], v[66:69], v234, v235 op_sel_hi:[0,0,0]
	s_setprio 0
	s_setprio 1
	v_mfma_scale_f32_16x16x128_f8f6f4 v[62:65], v[2:9], v[198:205], v[62:65], v234, v235 op_sel_hi:[0,0,0]
	v_mfma_scale_f32_16x16x128_f8f6f4 v[58:61], v[10:17], v[198:205], v[58:61], v234, v235 op_sel_hi:[0,0,0]
	v_mfma_scale_f32_16x16x128_f8f6f4 v[54:57], v[2:9], v[206:213], v[54:57], v234, v235 op_sel_hi:[0,0,0]
	v_mfma_scale_f32_16x16x128_f8f6f4 v[50:53], v[10:17], v[206:213], v[50:53], v234, v235 op_sel_hi:[0,0,0]
	v_mfma_scale_f32_16x16x128_f8f6f4 v[46:49], v[2:9], v[216:223], v[46:49], v234, v235 op_sel_hi:[0,0,0]
	v_mfma_scale_f32_16x16x128_f8f6f4 v[42:45], v[10:17], v[216:223], v[42:45], v234, v235 op_sel_hi:[0,0,0]
	v_mfma_scale_f32_16x16x128_f8f6f4 v[38:41], v[2:9], v[224:231], v[38:41], v234, v235 op_sel_hi:[0,0,0]
	v_mfma_scale_f32_16x16x128_f8f6f4 v[34:37], v[10:17], v[224:231], v[34:37], v234, v235 op_sel_hi:[0,0,0]
	s_setprio 0
	s_waitcnt vmcnt(8)
	s_barrier
	s_add_u32 s46, s46, 0x20180
	s_addc_u32 s47, s47, 0
	s_add_u32 s37, s44, 0x200
	s_addc_u32 s74, s45, 0
	s_mov_b32 s75, 0
.Lip8l_BB0_388:
	ds_read_b128 v[2:5], v180
	ds_read_b128 v[6:9], v181
	ds_read_b128 v[10:13], v182
	ds_read_b128 v[14:17], v183
	ds_read_b128 v[26:29], v184
	ds_read_b128 v[30:33], v185
	ds_read_b128 v[172:175], v186
	ds_read_b128 v[176:179], v187
	s_add_u32 s44, s46, 0xfffe0080
	s_addc_u32 s45, s47, -1
	s_cmp_eq_u32 s75, 4
	s_cselect_b32 s49, s1, s45
	s_cselect_b32 s48, s5, s44
	s_cselect_b32 s45, s23, s74
	s_cselect_b32 s44, s26, s37
	s_mov_b32 m0, s27
	v_lshl_add_u64 v[224:225], s[46:47], 0, v[168:169]
	ds_read_b128 v[18:21], v196
	ds_read_b128 v[22:25], v196 offset:1024
	ds_read_b128 v[198:201], v196 offset:2048
	ds_read_b128 v[202:205], v196 offset:3072
	ds_read_b128 v[206:209], v196 offset:4096
	ds_read_b128 v[210:213], v196 offset:5120
	ds_read_b128 v[216:219], v196 offset:6144
	ds_read_b128 v[220:223], v196 offset:7168
	global_load_lds_dwordx4 v[224:225], off
	v_lshl_add_u64 v[224:225], s[46:47], 0, v[170:171]
	s_mov_b32 m0, s35
	s_nop 0
	global_load_lds_dwordx4 v[224:225], off
	s_waitcnt lgkmcnt(0)
	s_barrier
	s_setprio 1
	s_waitcnt lgkmcnt(0)
	v_mfma_scale_f32_16x16x128_f8f6f4 v[158:161], v[2:9], v[18:25], v[158:161], v234, v235 op_sel_hi:[0,0,0]
	v_mfma_scale_f32_16x16x128_f8f6f4 v[154:157], v[10:17], v[18:25], v[154:157], v234, v235 op_sel_hi:[0,0,0]
	v_mfma_scale_f32_16x16x128_f8f6f4 v[150:153], v[2:9], v[198:205], v[150:153], v234, v235 op_sel_hi:[0,0,0]
	v_mfma_scale_f32_16x16x128_f8f6f4 v[146:149], v[10:17], v[198:205], v[146:149], v234, v235 op_sel_hi:[0,0,0]
	v_mfma_scale_f32_16x16x128_f8f6f4 v[142:145], v[2:9], v[206:213], v[142:145], v234, v235 op_sel_hi:[0,0,0]
	v_mfma_scale_f32_16x16x128_f8f6f4 v[138:141], v[10:17], v[206:213], v[138:141], v234, v235 op_sel_hi:[0,0,0]
	v_mfma_scale_f32_16x16x128_f8f6f4 v[134:137], v[2:9], v[216:223], v[134:137], v234, v235 op_sel_hi:[0,0,0]
	v_mfma_scale_f32_16x16x128_f8f6f4 v[130:133], v[10:17], v[216:223], v[130:133], v234, v235 op_sel_hi:[0,0,0]
	s_setprio 0
	s_setprio 1
	v_mfma_scale_f32_16x16x128_f8f6f4 v[126:129], v[26:33], v[18:25], v[126:129], v234, v235 op_sel_hi:[0,0,0]
	v_mfma_scale_f32_16x16x128_f8f6f4 v[122:125], v[172:179], v[18:25], v[122:125], v234, v235 op_sel_hi:[0,0,0]
	v_mfma_scale_f32_16x16x128_f8f6f4 v[118:121], v[26:33], v[198:205], v[118:121], v234, v235 op_sel_hi:[0,0,0]
	v_mfma_scale_f32_16x16x128_f8f6f4 v[114:117], v[172:179], v[198:205], v[114:117], v234, v235 op_sel_hi:[0,0,0]
	v_mfma_scale_f32_16x16x128_f8f6f4 v[110:113], v[26:33], v[206:213], v[110:113], v234, v235 op_sel_hi:[0,0,0]
	v_mfma_scale_f32_16x16x128_f8f6f4 v[106:109], v[172:179], v[206:213], v[106:109], v234, v235 op_sel_hi:[0,0,0]
	v_mfma_scale_f32_16x16x128_f8f6f4 v[102:105], v[26:33], v[216:223], v[102:105], v234, v235 op_sel_hi:[0,0,0]
	v_mfma_scale_f32_16x16x128_f8f6f4 v[98:101], v[172:179], v[216:223], v[98:101], v234, v235 op_sel_hi:[0,0,0]
	s_setprio 0
	s_waitcnt vmcnt(8)
	s_barrier
	s_mov_b32 m0, s58
	v_lshl_add_u64 v[18:19], s[44:45], 0, v[0:1]
	s_add_u32 vcc_lo, s44, 0x20000
	ds_read_b128 v[198:201], v196 offset:16384
	ds_read_b128 v[202:205], v196 offset:17408
	ds_read_b128 v[206:209], v196 offset:18432
	ds_read_b128 v[210:213], v196 offset:19456
	ds_read_b128 v[216:219], v196 offset:20480
	ds_read_b128 v[220:223], v196 offset:21504
	ds_read_b128 v[224:227], v196 offset:22528
	ds_read_b128 v[228:231], v196 offset:23552
	global_load_lds_dwordx4 v[18:19], off
	v_lshl_add_u64 v[20:21], s[44:45], 0, v[166:167]
	s_mov_b32 m0, s59
	s_addc_u32 vcc_hi, s45, 0
	global_load_lds_dwordx4 v[20:21], off
	v_lshl_add_u64 v[22:23], vcc, 0, v[0:1]
	s_mov_b32 m0, s60
	v_lshl_add_u64 v[24:25], s[48:49], 0, v[164:165]
	global_load_lds_dwordx4 v[22:23], off
	v_lshl_add_u64 v[22:23], vcc, 0, v[166:167]
	s_mov_b32 m0, s61
	s_nop 0
	global_load_lds_dwordx4 v[22:23], off
	v_lshl_add_u64 v[22:23], s[48:49], 0, v[162:163]
	s_mov_b32 m0, s57
	s_nop 0
	global_load_lds_dwordx4 v[22:23], off
	s_mov_b32 m0, s62
	s_nop 0
	global_load_lds_dwordx4 v[24:25], off
	s_waitcnt lgkmcnt(0)
	s_barrier
	s_setprio 1
	s_waitcnt lgkmcnt(0)
	v_mfma_scale_f32_16x16x128_f8f6f4 v[94:97], v[2:9], v[198:205], v[94:97], v234, v235 op_sel_hi:[0,0,0]
	v_mfma_scale_f32_16x16x128_f8f6f4 v[90:93], v[10:17], v[198:205], v[90:93], v234, v235 op_sel_hi:[0,0,0]
	v_mfma_scale_f32_16x16x128_f8f6f4 v[86:89], v[2:9], v[206:213], v[86:89], v234, v235 op_sel_hi:[0,0,0]
	v_mfma_scale_f32_16x16x128_f8f6f4 v[82:85], v[10:17], v[206:213], v[82:85], v234, v235 op_sel_hi:[0,0,0]
	v_mfma_scale_f32_16x16x128_f8f6f4 v[78:81], v[2:9], v[216:223], v[78:81], v234, v235 op_sel_hi:[0,0,0]
	v_mfma_scale_f32_16x16x128_f8f6f4 v[74:77], v[10:17], v[216:223], v[74:77], v234, v235 op_sel_hi:[0,0,0]
	v_mfma_scale_f32_16x16x128_f8f6f4 v[70:73], v[2:9], v[224:231], v[70:73], v234, v235 op_sel_hi:[0,0,0]
	v_mfma_scale_f32_16x16x128_f8f6f4 v[66:69], v[10:17], v[224:231], v[66:69], v234, v235 op_sel_hi:[0,0,0]
	s_setprio 0
	s_setprio 1
	v_mfma_scale_f32_16x16x128_f8f6f4 v[62:65], v[26:33], v[198:205], v[62:65], v234, v235 op_sel_hi:[0,0,0]
	v_mfma_scale_f32_16x16x128_f8f6f4 v[58:61], v[172:179], v[198:205], v[58:61], v234, v235 op_sel_hi:[0,0,0]
	v_mfma_scale_f32_16x16x128_f8f6f4 v[54:57], v[26:33], v[206:213], v[54:57], v234, v235 op_sel_hi:[0,0,0]
	v_mfma_scale_f32_16x16x128_f8f6f4 v[50:53], v[172:179], v[206:213], v[50:53], v234, v235 op_sel_hi:[0,0,0]
	v_mfma_scale_f32_16x16x128_f8f6f4 v[46:49], v[26:33], v[216:223], v[46:49], v234, v235 op_sel_hi:[0,0,0]
	v_mfma_scale_f32_16x16x128_f8f6f4 v[42:45], v[172:179], v[216:223], v[42:45], v234, v235 op_sel_hi:[0,0,0]
	v_mfma_scale_f32_16x16x128_f8f6f4 v[38:41], v[26:33], v[224:231], v[38:41], v234, v235 op_sel_hi:[0,0,0]
	v_mfma_scale_f32_16x16x128_f8f6f4 v[34:37], v[172:179], v[224:231], v[34:37], v234, v235 op_sel_hi:[0,0,0]
	s_setprio 0
	s_waitcnt vmcnt(8)
	s_barrier
	ds_read_b128 v[10:13], v188
	ds_read_b128 v[14:17], v189
	ds_read_b128 v[26:29], v190
	ds_read_b128 v[30:33], v191
	ds_read_b128 v[2:5], v192
	ds_read_b128 v[6:9], v193
	ds_read_b128 v[172:175], v194
	ds_read_b128 v[176:179], v195
	s_add_u32 s48, s48, 0x20000
	s_addc_u32 s49, s49, 0
	s_mov_b32 m0, s63
	v_lshl_add_u64 v[232:233], s[48:49], 0, v[162:163]
	ds_read_b128 v[198:201], v196 offset:32768
	ds_read_b128 v[202:205], v196 offset:33792
	ds_read_b128 v[206:209], v196 offset:34816
	ds_read_b128 v[210:213], v196 offset:35840
	ds_read_b128 v[216:219], v196 offset:36864
	ds_read_b128 v[220:223], v196 offset:37888
	ds_read_b128 v[224:227], v196 offset:38912
	ds_read_b128 v[228:231], v196 offset:39936
	global_load_lds_dwordx4 v[232:233], off
	v_lshl_add_u64 v[232:233], s[48:49], 0, v[164:165]
	s_mov_b32 m0, s64
	s_nop 0
	global_load_lds_dwordx4 v[232:233], off
	s_waitcnt lgkmcnt(0)
	s_barrier
	s_setprio 1
	s_waitcnt lgkmcnt(0)
	v_mfma_scale_f32_16x16x128_f8f6f4 v[158:161], v[10:17], v[198:205], v[158:161], v234, v235 op_sel_hi:[0,0,0]
	v_mfma_scale_f32_16x16x128_f8f6f4 v[154:157], v[26:33], v[198:205], v[154:157], v234, v235 op_sel_hi:[0,0,0]
	v_mfma_scale_f32_16x16x128_f8f6f4 v[150:153], v[10:17], v[206:213], v[150:153], v234, v235 op_sel_hi:[0,0,0]
	v_mfma_scale_f32_16x16x128_f8f6f4 v[146:149], v[26:33], v[206:213], v[146:149], v234, v235 op_sel_hi:[0,0,0]
	v_mfma_scale_f32_16x16x128_f8f6f4 v[142:145], v[10:17], v[216:223], v[142:145], v234, v235 op_sel_hi:[0,0,0]
	v_mfma_scale_f32_16x16x128_f8f6f4 v[138:141], v[26:33], v[216:223], v[138:141], v234, v235 op_sel_hi:[0,0,0]
	v_mfma_scale_f32_16x16x128_f8f6f4 v[134:137], v[10:17], v[224:231], v[134:137], v234, v235 op_sel_hi:[0,0,0]
	v_mfma_scale_f32_16x16x128_f8f6f4 v[130:133], v[26:33], v[224:231], v[130:133], v234, v235 op_sel_hi:[0,0,0]
	s_setprio 0
	s_setprio 1
	v_mfma_scale_f32_16x16x128_f8f6f4 v[126:129], v[2:9], v[198:205], v[126:129], v234, v235 op_sel_hi:[0,0,0]
	v_mfma_scale_f32_16x16x128_f8f6f4 v[122:125], v[172:179], v[198:205], v[122:125], v234, v235 op_sel_hi:[0,0,0]
	v_mfma_scale_f32_16x16x128_f8f6f4 v[118:121], v[2:9], v[206:213], v[118:121], v234, v235 op_sel_hi:[0,0,0]
	v_mfma_scale_f32_16x16x128_f8f6f4 v[114:117], v[172:179], v[206:213], v[114:117], v234, v235 op_sel_hi:[0,0,0]
	v_mfma_scale_f32_16x16x128_f8f6f4 v[110:113], v[2:9], v[216:223], v[110:113], v234, v235 op_sel_hi:[0,0,0]
	v_mfma_scale_f32_16x16x128_f8f6f4 v[106:109], v[172:179], v[216:223], v[106:109], v234, v235 op_sel_hi:[0,0,0]
	v_mfma_scale_f32_16x16x128_f8f6f4 v[102:105], v[2:9], v[224:231], v[102:105], v234, v235 op_sel_hi:[0,0,0]
	v_mfma_scale_f32_16x16x128_f8f6f4 v[98:101], v[172:179], v[224:231], v[98:101], v234, v235 op_sel_hi:[0,0,0]
	s_setprio 0
	s_waitcnt vmcnt(8)
	s_barrier
	s_mov_b32 m0, s7
	v_lshl_add_u64 v[18:19], v[18:19], 0, s[66:67]
	s_add_u32 s44, s44, 0x20080
	ds_read_b128 v[198:201], v196 offset:49152
	ds_read_b128 v[202:205], v196 offset:50176
	ds_read_b128 v[206:209], v196 offset:51200
	ds_read_b128 v[210:213], v196 offset:52224
	ds_read_b128 v[216:219], v196 offset:53248
	ds_read_b128 v[220:223], v196 offset:54272
	ds_read_b128 v[224:227], v196 offset:55296
	ds_read_b128 v[228:231], v196 offset:56320
	global_load_lds_dwordx4 v[18:19], off
	v_lshl_add_u64 v[18:19], v[20:21], 0, s[66:67]
	s_mov_b32 m0, s65
	s_addc_u32 s45, s45, 0
	global_load_lds_dwordx4 v[18:19], off
	v_lshl_add_u64 v[18:19], s[44:45], 0, v[0:1]
	s_mov_b32 m0, s13
	s_nop 0
	global_load_lds_dwordx4 v[18:19], off
	v_lshl_add_u64 v[18:19], s[44:45], 0, v[166:167]
	s_mov_b32 m0, s51
	s_nop 0
	global_load_lds_dwordx4 v[18:19], off
	v_lshl_add_u64 v[18:19], v[22:23], 0, s[66:67]
	s_mov_b32 m0, s68
	s_nop 0
	global_load_lds_dwordx4 v[18:19], off
	v_lshl_add_u64 v[18:19], v[24:25], 0, s[66:67]
	s_mov_b32 m0, s52
	s_nop 0
	global_load_lds_dwordx4 v[18:19], off
	s_waitcnt lgkmcnt(0)
	s_barrier
	s_setprio 1
	s_waitcnt lgkmcnt(0)
	v_mfma_scale_f32_16x16x128_f8f6f4 v[94:97], v[10:17], v[198:205], v[94:97], v234, v235 op_sel_hi:[0,0,0]
	v_mfma_scale_f32_16x16x128_f8f6f4 v[90:93], v[26:33], v[198:205], v[90:93], v234, v235 op_sel_hi:[0,0,0]
	v_mfma_scale_f32_16x16x128_f8f6f4 v[86:89], v[10:17], v[206:213], v[86:89], v234, v235 op_sel_hi:[0,0,0]
	v_mfma_scale_f32_16x16x128_f8f6f4 v[82:85], v[26:33], v[206:213], v[82:85], v234, v235 op_sel_hi:[0,0,0]
	v_mfma_scale_f32_16x16x128_f8f6f4 v[78:81], v[10:17], v[216:223], v[78:81], v234, v235 op_sel_hi:[0,0,0]
	v_mfma_scale_f32_16x16x128_f8f6f4 v[74:77], v[26:33], v[216:223], v[74:77], v234, v235 op_sel_hi:[0,0,0]
	v_mfma_scale_f32_16x16x128_f8f6f4 v[70:73], v[10:17], v[224:231], v[70:73], v234, v235 op_sel_hi:[0,0,0]
	v_mfma_scale_f32_16x16x128_f8f6f4 v[66:69], v[26:33], v[224:231], v[66:69], v234, v235 op_sel_hi:[0,0,0]
	s_setprio 0
	s_setprio 1
	v_mfma_scale_f32_16x16x128_f8f6f4 v[62:65], v[2:9], v[198:205], v[62:65], v234, v235 op_sel_hi:[0,0,0]
	v_mfma_scale_f32_16x16x128_f8f6f4 v[58:61], v[172:179], v[198:205], v[58:61], v234, v235 op_sel_hi:[0,0,0]
	v_mfma_scale_f32_16x16x128_f8f6f4 v[54:57], v[2:9], v[206:213], v[54:57], v234, v235 op_sel_hi:[0,0,0]
	v_mfma_scale_f32_16x16x128_f8f6f4 v[50:53], v[172:179], v[206:213], v[50:53], v234, v235 op_sel_hi:[0,0,0]
	v_mfma_scale_f32_16x16x128_f8f6f4 v[46:49], v[2:9], v[216:223], v[46:49], v234, v235 op_sel_hi:[0,0,0]
	v_mfma_scale_f32_16x16x128_f8f6f4 v[42:45], v[172:179], v[216:223], v[42:45], v234, v235 op_sel_hi:[0,0,0]
	v_mfma_scale_f32_16x16x128_f8f6f4 v[38:41], v[2:9], v[224:231], v[38:41], v234, v235 op_sel_hi:[0,0,0]
	v_mfma_scale_f32_16x16x128_f8f6f4 v[34:37], v[172:179], v[224:231], v[34:37], v234, v235 op_sel_hi:[0,0,0]
	s_setprio 0
	s_waitcnt vmcnt(8)
	s_barrier
	s_add_i32 s75, s75, 2
	s_add_u32 s46, s46, 0x100
	s_addc_u32 s47, s47, 0
	s_add_u32 s37, s37, 0x100
	s_addc_u32 s74, s74, 0
	s_cmp_gt_u32 s75, 5
	s_cbranch_scc0 .Lip8l_BB0_388
.Lip8_join:
	s_and_b64 vcc, exec, s[30:31]
	s_cbranch_vccz .LBB0_391
	s_barrier

.LBB0_2001:
	ds_read_b128 v[6:9], v176
	ds_read_b128 v[2:5], v177
	ds_read_b128 v[14:17], v178
	ds_read_b128 v[10:13], v179
	ds_read_b128 v[22:25], v180
	ds_read_b128 v[18:21], v181
	ds_read_b128 v[30:33], v182
	ds_read_b128 v[26:29], v183
	s_lshl_b32 s26, s31, 10
	s_and_b32 s26, s26, 0x400
	s_add_i32 s26, s26, 0
	s_add_i32 s26, s26, 0x23000
	v_lshlrev_b32_e32 v0, 10, v196
	s_add_i32 s27, s65, 0xc000
	v_and_or_b32 v166, v0, s82, v174
	v_bfe_u32 v0, v196, 16, 16
	s_mov_b32 m0, s27
	s_add_i32 s41, s65, 0xe000
	ds_read_b128 v[198:201], v192
	ds_read_b128 v[202:205], v192 offset:1024
	ds_read_b128 v[206:209], v192 offset:2048
	ds_read_b128 v[210:213], v192 offset:3072
	ds_read_b128 v[216:219], v192 offset:4096
	ds_read_b128 v[220:223], v192 offset:5120
	ds_read_b128 v[224:227], v192 offset:6144
	ds_read_b128 v[228:231], v192 offset:7168
	v_lshl_add_u32 v168, v0, 10, v175
	global_load_lds_dwordx4 v166, s[28:29]
	s_mov_b32 m0, s41
	v_mov_b32_e32 v167, v1
	global_load_lds_dwordx4 v168, s[28:29]
	v_readlane_b32 s100, v254, 51
	v_readlane_b32 s101, v254, 52
	s_cmp_lg_u64 s[100:101], 0
	s_cbranch_scc1 .Lg1l_start
	s_cmp_eq_u32 s23, 0
	s_cbranch_scc1 .Lrw_first_g1_0
	s_waitcnt vmcnt(12)
	s_branch .Lrw_done_g1_0

.Lg1l_start:
	s_waitcnt lgkmcnt(0)
	v_mov_b32_e32 v169, v1
	s_barrier
	s_setprio 1
	s_waitcnt lgkmcnt(0)
	v_mfma_scale_f32_16x16x128_f8f6f4 v[150:153], v[26:33], v[198:205], 0, v234, v235 op_sel_hi:[0,0,0]
	v_mfma_scale_f32_16x16x128_f8f6f4 v[146:149], v[18:25], v[198:205], 0, v234, v235 op_sel_hi:[0,0,0]
	v_mfma_scale_f32_16x16x128_f8f6f4 v[142:145], v[26:33], v[206:213], 0, v234, v235 op_sel_hi:[0,0,0]
	v_mfma_scale_f32_16x16x128_f8f6f4 v[138:141], v[18:25], v[206:213], 0, v234, v235 op_sel_hi:[0,0,0]
	v_mfma_scale_f32_16x16x128_f8f6f4 v[134:137], v[26:33], v[216:223], 0, v234, v235 op_sel_hi:[0,0,0]
	v_mfma_scale_f32_16x16x128_f8f6f4 v[130:133], v[18:25], v[216:223], 0, v234, v235 op_sel_hi:[0,0,0]
	v_mfma_scale_f32_16x16x128_f8f6f4 v[126:129], v[26:33], v[224:231], 0, v234, v235 op_sel_hi:[0,0,0]
	v_mfma_scale_f32_16x16x128_f8f6f4 v[122:125], v[18:25], v[224:231], 0, v234, v235 op_sel_hi:[0,0,0]
	s_setprio 0
	s_setprio 1
	v_mfma_scale_f32_16x16x128_f8f6f4 v[118:121], v[10:17], v[198:205], 0, v234, v235 op_sel_hi:[0,0,0]
	v_mfma_scale_f32_16x16x128_f8f6f4 v[114:117], v[2:9], v[198:205], 0, v234, v235 op_sel_hi:[0,0,0]
	v_mfma_scale_f32_16x16x128_f8f6f4 v[110:113], v[10:17], v[206:213], 0, v234, v235 op_sel_hi:[0,0,0]
	v_mfma_scale_f32_16x16x128_f8f6f4 v[106:109], v[2:9], v[206:213], 0, v234, v235 op_sel_hi:[0,0,0]
	v_mfma_scale_f32_16x16x128_f8f6f4 v[102:105], v[10:17], v[216:223], 0, v234, v235 op_sel_hi:[0,0,0]
	v_mfma_scale_f32_16x16x128_f8f6f4 v[98:101], v[2:9], v[216:223], 0, v234, v235 op_sel_hi:[0,0,0]
	v_mfma_scale_f32_16x16x128_f8f6f4 v[94:97], v[10:17], v[224:231], 0, v234, v235 op_sel_hi:[0,0,0]
	v_mfma_scale_f32_16x16x128_f8f6f4 v[90:93], v[2:9], v[224:231], 0, v234, v235 op_sel_hi:[0,0,0]
	s_setprio 0
	s_cmp_eq_u32 s23, 0
	s_cbranch_scc1 .Lg1l_rw_first_g1_0
	s_waitcnt vmcnt(12)
	s_branch .Lg1l_rw_done_g1_0

.Lg1l_rw_done_g1_0:
	s_barrier
	v_lshl_add_u64 v[170:171], s[4:5], 0, v[162:163]
	s_mov_b64 s[54:55], 0x100
	s_mov_b32 m0, s68
	v_lshl_add_u64 v[172:173], v[170:171], 0, s[54:55]
	ds_read_b128 v[198:201], v192 offset:16384
	ds_read_b128 v[202:205], v192 offset:17408
	ds_read_b128 v[206:209], v192 offset:18432
	ds_read_b128 v[210:213], v192 offset:19456
	ds_read_b128 v[216:219], v192 offset:20480
	ds_read_b128 v[220:223], v192 offset:21504
	ds_read_b128 v[224:227], v192 offset:22528
	ds_read_b128 v[228:231], v192 offset:23552
	global_load_lds_dwordx4 v[172:173], off
	v_lshl_add_u64 v[172:173], s[4:5], 0, v[164:165]
	v_lshl_add_u64 v[232:233], v[172:173], 0, s[54:55]
	s_add_u32 s54, s4, 0x20100
	s_mov_b32 m0, s60
	s_addc_u32 s55, s5, 0
	global_load_lds_dwordx4 v[232:233], off
	v_lshl_add_u64 v[232:233], s[54:55], 0, v[162:163]
	s_mov_b32 m0, s61
	v_lshlrev_b32_e32 v0, 10, v195
	global_load_lds_dwordx4 v[232:233], off
	v_lshl_add_u64 v[232:233], s[54:55], 0, v[164:165]
	s_mov_b32 m0, s62
	v_and_or_b32 v0, v0, s82, v174
	global_load_lds_dwordx4 v[232:233], off
	v_bfe_u32 v197, v195, 16, 16
	s_mov_b32 m0, s65
	v_lshl_add_u32 v197, v197, 10, v175
	global_load_lds_dwordx4 v0, s[34:35]
	s_mov_b32 m0, s63
	s_nop 0
	global_load_lds_dwordx4 v197, s[34:35]
	s_waitcnt lgkmcnt(0)
	s_barrier
	s_setprio 1
	s_waitcnt lgkmcnt(0)
	v_mfma_scale_f32_16x16x128_f8f6f4 v[86:89], v[26:33], v[198:205], 0, v234, v235 op_sel_hi:[0,0,0]
	v_mfma_scale_f32_16x16x128_f8f6f4 v[82:85], v[18:25], v[198:205], 0, v234, v235 op_sel_hi:[0,0,0]
	v_mfma_scale_f32_16x16x128_f8f6f4 v[78:81], v[26:33], v[206:213], 0, v234, v235 op_sel_hi:[0,0,0]
	v_mfma_scale_f32_16x16x128_f8f6f4 v[74:77], v[18:25], v[206:213], 0, v234, v235 op_sel_hi:[0,0,0]
	v_mfma_scale_f32_16x16x128_f8f6f4 v[70:73], v[26:33], v[216:223], 0, v234, v235 op_sel_hi:[0,0,0]
	v_mfma_scale_f32_16x16x128_f8f6f4 v[66:69], v[18:25], v[216:223], 0, v234, v235 op_sel_hi:[0,0,0]
	v_mfma_scale_f32_16x16x128_f8f6f4 v[62:65], v[26:33], v[224:231], 0, v234, v235 op_sel_hi:[0,0,0]
	v_mfma_scale_f32_16x16x128_f8f6f4 v[58:61], v[18:25], v[224:231], 0, v234, v235 op_sel_hi:[0,0,0]
	s_setprio 0
	s_setprio 1
	v_mfma_scale_f32_16x16x128_f8f6f4 v[54:57], v[10:17], v[198:205], 0, v234, v235 op_sel_hi:[0,0,0]
	v_mfma_scale_f32_16x16x128_f8f6f4 v[50:53], v[2:9], v[198:205], 0, v234, v235 op_sel_hi:[0,0,0]
	v_mfma_scale_f32_16x16x128_f8f6f4 v[46:49], v[10:17], v[206:213], 0, v234, v235 op_sel_hi:[0,0,0]
	v_mfma_scale_f32_16x16x128_f8f6f4 v[42:45], v[2:9], v[206:213], 0, v234, v235 op_sel_hi:[0,0,0]
	v_mfma_scale_f32_16x16x128_f8f6f4 v[38:41], v[10:17], v[216:223], 0, v234, v235 op_sel_hi:[0,0,0]
	v_mfma_scale_f32_16x16x128_f8f6f4 v[34:37], v[2:9], v[216:223], 0, v234, v235 op_sel_hi:[0,0,0]
	v_mfma_scale_f32_16x16x128_f8f6f4 v[154:157], v[10:17], v[224:231], 0, v234, v235 op_sel_hi:[0,0,0]
	v_mfma_scale_f32_16x16x128_f8f6f4 v[158:161], v[2:9], v[224:231], 0, v234, v235 op_sel_hi:[0,0,0]
	s_setprio 0
	s_cmp_eq_u32 s23, 0
	s_cbranch_scc1 .Lg1l_rw_first_g1_1
	s_waitcnt vmcnt(12)
	s_branch .Lg1l_rw_done_g1_1

.Lg1l_rw_done_g1_1:
	s_barrier
	ds_read_b128 v[18:21], v184
	ds_read_b128 v[22:25], v185
	ds_read_b128 v[26:29], v186
	ds_read_b128 v[30:33], v187
	ds_read_b128 v[2:5], v188
	ds_read_b128 v[6:9], v189
	ds_read_b128 v[10:13], v190
	ds_read_b128 v[14:17], v191
	s_mov_b32 m0, s10
	ds_read_b128 v[198:201], v192 offset:32768
	ds_read_b128 v[202:205], v192 offset:33792
	ds_read_b128 v[206:209], v192 offset:34816
	ds_read_b128 v[210:213], v192 offset:35840
	ds_read_b128 v[216:219], v192 offset:36864
	ds_read_b128 v[220:223], v192 offset:37888
	ds_read_b128 v[224:227], v192 offset:38912
	ds_read_b128 v[228:231], v192 offset:39936
	global_load_lds_dwordx4 v166, s[34:35]
	s_mov_b32 m0, s11
	s_nop 0
	global_load_lds_dwordx4 v168, s[34:35]
	s_waitcnt lgkmcnt(0)
	s_barrier
	s_setprio 1
	s_waitcnt lgkmcnt(0)
	v_mfma_scale_f32_16x16x128_f8f6f4 v[150:153], v[18:25], v[198:205], v[150:153], v234, v235 op_sel_hi:[0,0,0]
	v_mfma_scale_f32_16x16x128_f8f6f4 v[146:149], v[26:33], v[198:205], v[146:149], v234, v235 op_sel_hi:[0,0,0]
	v_mfma_scale_f32_16x16x128_f8f6f4 v[142:145], v[18:25], v[206:213], v[142:145], v234, v235 op_sel_hi:[0,0,0]
	v_mfma_scale_f32_16x16x128_f8f6f4 v[138:141], v[26:33], v[206:213], v[138:141], v234, v235 op_sel_hi:[0,0,0]
	v_mfma_scale_f32_16x16x128_f8f6f4 v[134:137], v[18:25], v[216:223], v[134:137], v234, v235 op_sel_hi:[0,0,0]
	v_mfma_scale_f32_16x16x128_f8f6f4 v[130:133], v[26:33], v[216:223], v[130:133], v234, v235 op_sel_hi:[0,0,0]
	v_mfma_scale_f32_16x16x128_f8f6f4 v[126:129], v[18:25], v[224:231], v[126:129], v234, v235 op_sel_hi:[0,0,0]
	v_mfma_scale_f32_16x16x128_f8f6f4 v[122:125], v[26:33], v[224:231], v[122:125], v234, v235 op_sel_hi:[0,0,0]
	s_setprio 0
	s_setprio 1
	v_mfma_scale_f32_16x16x128_f8f6f4 v[118:121], v[2:9], v[198:205], v[118:121], v234, v235 op_sel_hi:[0,0,0]
	v_mfma_scale_f32_16x16x128_f8f6f4 v[114:117], v[10:17], v[198:205], v[114:117], v234, v235 op_sel_hi:[0,0,0]
	v_mfma_scale_f32_16x16x128_f8f6f4 v[110:113], v[2:9], v[206:213], v[110:113], v234, v235 op_sel_hi:[0,0,0]
	v_mfma_scale_f32_16x16x128_f8f6f4 v[106:109], v[10:17], v[206:213], v[106:109], v234, v235 op_sel_hi:[0,0,0]
	v_mfma_scale_f32_16x16x128_f8f6f4 v[102:105], v[2:9], v[216:223], v[102:105], v234, v235 op_sel_hi:[0,0,0]
	v_mfma_scale_f32_16x16x128_f8f6f4 v[98:101], v[10:17], v[216:223], v[98:101], v234, v235 op_sel_hi:[0,0,0]
	v_mfma_scale_f32_16x16x128_f8f6f4 v[94:97], v[2:9], v[224:231], v[94:97], v234, v235 op_sel_hi:[0,0,0]
	v_mfma_scale_f32_16x16x128_f8f6f4 v[90:93], v[10:17], v[224:231], v[90:93], v234, v235 op_sel_hi:[0,0,0]
	s_setprio 0
	s_waitcnt vmcnt(8)
	s_barrier
	s_mov_b64 s[54:55], 0x180
	s_mov_b32 m0, s64
	v_lshl_add_u64 v[170:171], v[170:171], 0, s[54:55]
	ds_read_b128 v[198:201], v192 offset:49152
	ds_read_b128 v[202:205], v192 offset:50176
	ds_read_b128 v[206:209], v192 offset:51200
	ds_read_b128 v[210:213], v192 offset:52224
	ds_read_b128 v[216:219], v192 offset:53248
	ds_read_b128 v[220:223], v192 offset:54272
	ds_read_b128 v[224:227], v192 offset:55296
	ds_read_b128 v[228:231], v192 offset:56320
	global_load_lds_dwordx4 v[170:171], off
	v_lshl_add_u64 v[170:171], v[172:173], 0, s[54:55]
	s_add_u32 s54, s4, 0x20180
	s_mov_b32 m0, s81
	s_addc_u32 s55, s5, 0
	global_load_lds_dwordx4 v[170:171], off
	v_lshl_add_u64 v[170:171], s[54:55], 0, v[162:163]
	s_mov_b32 m0, s49
	s_nop 0
	global_load_lds_dwordx4 v[170:171], off
	v_lshl_add_u64 v[170:171], s[54:55], 0, v[164:165]
	s_mov_b32 m0, s30
	s_nop 0
	global_load_lds_dwordx4 v[170:171], off
	s_mov_b32 m0, s6
	s_nop 0
	global_load_lds_dwordx4 v0, s[36:37]
	s_mov_b32 m0, s7
	s_nop 0
	global_load_lds_dwordx4 v197, s[36:37]
	s_waitcnt lgkmcnt(0)
	s_barrier
	s_setprio 1
	s_waitcnt lgkmcnt(0)
	v_mfma_scale_f32_16x16x128_f8f6f4 v[86:89], v[18:25], v[198:205], v[86:89], v234, v235 op_sel_hi:[0,0,0]
	v_mfma_scale_f32_16x16x128_f8f6f4 v[82:85], v[26:33], v[198:205], v[82:85], v234, v235 op_sel_hi:[0,0,0]
	v_mfma_scale_f32_16x16x128_f8f6f4 v[78:81], v[18:25], v[206:213], v[78:81], v234, v235 op_sel_hi:[0,0,0]
	v_mfma_scale_f32_16x16x128_f8f6f4 v[74:77], v[26:33], v[206:213], v[74:77], v234, v235 op_sel_hi:[0,0,0]
	v_mfma_scale_f32_16x16x128_f8f6f4 v[70:73], v[18:25], v[216:223], v[70:73], v234, v235 op_sel_hi:[0,0,0]
	v_mfma_scale_f32_16x16x128_f8f6f4 v[66:69], v[26:33], v[216:223], v[66:69], v234, v235 op_sel_hi:[0,0,0]
	v_mfma_scale_f32_16x16x128_f8f6f4 v[62:65], v[18:25], v[224:231], v[62:65], v234, v235 op_sel_hi:[0,0,0]
	v_mfma_scale_f32_16x16x128_f8f6f4 v[58:61], v[26:33], v[224:231], v[58:61], v234, v235 op_sel_hi:[0,0,0]
	s_setprio 0
	s_setprio 1
	v_mfma_scale_f32_16x16x128_f8f6f4 v[54:57], v[2:9], v[198:205], v[54:57], v234, v235 op_sel_hi:[0,0,0]
	v_mfma_scale_f32_16x16x128_f8f6f4 v[50:53], v[10:17], v[198:205], v[50:53], v234, v235 op_sel_hi:[0,0,0]
	v_mfma_scale_f32_16x16x128_f8f6f4 v[46:49], v[2:9], v[206:213], v[46:49], v234, v235 op_sel_hi:[0,0,0]
	v_mfma_scale_f32_16x16x128_f8f6f4 v[42:45], v[10:17], v[206:213], v[42:45], v234, v235 op_sel_hi:[0,0,0]
	v_mfma_scale_f32_16x16x128_f8f6f4 v[38:41], v[2:9], v[216:223], v[38:41], v234, v235 op_sel_hi:[0,0,0]
	v_mfma_scale_f32_16x16x128_f8f6f4 v[34:37], v[10:17], v[216:223], v[34:37], v234, v235 op_sel_hi:[0,0,0]
	v_mfma_scale_f32_16x16x128_f8f6f4 v[154:157], v[2:9], v[224:231], v[154:157], v234, v235 op_sel_hi:[0,0,0]
	v_mfma_scale_f32_16x16x128_f8f6f4 v[158:161], v[10:17], v[224:231], v[158:161], v234, v235 op_sel_hi:[0,0,0]
	s_setprio 0
	s_waitcnt vmcnt(8)
	s_barrier
	s_add_u32 s43, s4, 0x200
	s_addc_u32 s45, s5, 0
	s_mov_b32 s74, 0
	s_mov_b64 s[54:55], s[36:37]
	s_branch .Lg1l_BB0_2003
.Lg1l_BB0_2002:
	ds_read_b128 v[2:5], v183
	ds_read_b128 v[6:9], v182
	ds_read_b128 v[10:13], v181
	ds_read_b128 v[14:17], v180
	ds_read_b128 v[26:29], v179
	ds_read_b128 v[30:33], v178
	ds_read_b128 v[198:201], v177
	ds_read_b128 v[202:205], v176
	s_add_u32 s58, s54, 0x80
	s_addc_u32 s59, s55, 0
	s_and_b64 s[56:57], s[4:5], exec
	s_cselect_b32 s59, s9, s59
	s_cselect_b32 s58, s8, s58
	s_cselect_b32 s57, s47, s45
	s_cselect_b32 s56, s46, s43
	s_mov_b32 m0, s27
	v_lshl_add_u64 v[170:171], s[54:55], 0, v[166:167]
	ds_read_b128 v[18:21], v192
	ds_read_b128 v[22:25], v192 offset:1024
	ds_read_b128 v[206:209], v192 offset:2048
	ds_read_b128 v[210:213], v192 offset:3072
	ds_read_b128 v[216:219], v192 offset:4096
	ds_read_b128 v[220:223], v192 offset:5120
	ds_read_b128 v[224:227], v192 offset:6144
	ds_read_b128 v[228:231], v192 offset:7168
	global_load_lds_dwordx4 v[170:171], off
	v_lshl_add_u64 v[170:171], s[54:55], 0, v[168:169]
	s_mov_b32 m0, s41
	s_nop 0
	global_load_lds_dwordx4 v[170:171], off
	s_waitcnt lgkmcnt(0)
	s_barrier
	s_setprio 1
	s_waitcnt lgkmcnt(0)
	v_mfma_scale_f32_16x16x128_f8f6f4 v[150:153], v[2:9], v[18:25], v[150:153], v234, v235 op_sel_hi:[0,0,0]
	v_mfma_scale_f32_16x16x128_f8f6f4 v[146:149], v[10:17], v[18:25], v[146:149], v234, v235 op_sel_hi:[0,0,0]
	v_mfma_scale_f32_16x16x128_f8f6f4 v[142:145], v[2:9], v[206:213], v[142:145], v234, v235 op_sel_hi:[0,0,0]
	v_mfma_scale_f32_16x16x128_f8f6f4 v[138:141], v[10:17], v[206:213], v[138:141], v234, v235 op_sel_hi:[0,0,0]
	v_mfma_scale_f32_16x16x128_f8f6f4 v[134:137], v[2:9], v[216:223], v[134:137], v234, v235 op_sel_hi:[0,0,0]
	v_mfma_scale_f32_16x16x128_f8f6f4 v[130:133], v[10:17], v[216:223], v[130:133], v234, v235 op_sel_hi:[0,0,0]
	v_mfma_scale_f32_16x16x128_f8f6f4 v[126:129], v[2:9], v[224:231], v[126:129], v234, v235 op_sel_hi:[0,0,0]
	v_mfma_scale_f32_16x16x128_f8f6f4 v[122:125], v[10:17], v[224:231], v[122:125], v234, v235 op_sel_hi:[0,0,0]
	s_setprio 0
	s_setprio 1
	v_mfma_scale_f32_16x16x128_f8f6f4 v[118:121], v[26:33], v[18:25], v[118:121], v234, v235 op_sel_hi:[0,0,0]
	v_mfma_scale_f32_16x16x128_f8f6f4 v[114:117], v[198:205], v[18:25], v[114:117], v234, v235 op_sel_hi:[0,0,0]
	v_mfma_scale_f32_16x16x128_f8f6f4 v[110:113], v[26:33], v[206:213], v[110:113], v234, v235 op_sel_hi:[0,0,0]
	v_mfma_scale_f32_16x16x128_f8f6f4 v[106:109], v[198:205], v[206:213], v[106:109], v234, v235 op_sel_hi:[0,0,0]
	v_mfma_scale_f32_16x16x128_f8f6f4 v[102:105], v[26:33], v[216:223], v[102:105], v234, v235 op_sel_hi:[0,0,0]
	v_mfma_scale_f32_16x16x128_f8f6f4 v[98:101], v[198:205], v[216:223], v[98:101], v234, v235 op_sel_hi:[0,0,0]
	v_mfma_scale_f32_16x16x128_f8f6f4 v[94:97], v[26:33], v[224:231], v[94:97], v234, v235 op_sel_hi:[0,0,0]
	v_mfma_scale_f32_16x16x128_f8f6f4 v[90:93], v[198:205], v[224:231], v[90:93], v234, v235 op_sel_hi:[0,0,0]
	s_setprio 0
	s_waitcnt vmcnt(8)
	s_barrier
	s_mov_b32 m0, s68
	v_lshl_add_u64 v[18:19], s[56:57], 0, v[162:163]
	s_add_u32 vcc_lo, s56, 0x20000
	ds_read_b128 v[206:209], v192 offset:16384
	ds_read_b128 v[210:213], v192 offset:17408
	ds_read_b128 v[216:219], v192 offset:18432
	ds_read_b128 v[220:223], v192 offset:19456
	ds_read_b128 v[224:227], v192 offset:20480
	ds_read_b128 v[228:231], v192 offset:21504
	ds_read_b128 v[244:247], v192 offset:22528
	ds_read_b128 v[248:251], v192 offset:23552
	global_load_lds_dwordx4 v[18:19], off
	v_lshl_add_u64 v[20:21], s[56:57], 0, v[164:165]
	s_mov_b32 m0, s60
	s_addc_u32 vcc_hi, s57, 0
	global_load_lds_dwordx4 v[20:21], off
	v_lshl_add_u64 v[22:23], vcc, 0, v[162:163]
	s_mov_b32 m0, s61
	s_nop 0
	global_load_lds_dwordx4 v[22:23], off
	v_lshl_add_u64 v[22:23], vcc, 0, v[164:165]
	s_mov_b32 m0, s62
	s_nop 0
	global_load_lds_dwordx4 v[22:23], off
	v_cndmask_b32_e64 v22, v195, v193, s[4:5]
	v_lshlrev_b32_e32 v0, 10, v22
	v_and_or_b32 v0, v0, s82, v174
	v_bfe_u32 v22, v22, 16, 16
	s_mov_b32 m0, s65
	v_lshl_add_u32 v22, v22, 10, v175
	global_load_lds_dwordx4 v0, s[58:59]
	s_mov_b32 m0, s63
	v_mov_b32_e32 v23, v1
	global_load_lds_dwordx4 v22, s[58:59]
	s_waitcnt lgkmcnt(0)
	v_lshl_add_u64 v[24:25], s[58:59], 0, v[0:1]
	v_lshl_add_u64 v[22:23], s[58:59], 0, v[22:23]
	s_barrier
	s_setprio 1
	s_waitcnt lgkmcnt(0)
	v_mfma_scale_f32_16x16x128_f8f6f4 v[86:89], v[2:9], v[206:213], v[86:89], v234, v235 op_sel_hi:[0,0,0]
	v_mfma_scale_f32_16x16x128_f8f6f4 v[82:85], v[10:17], v[206:213], v[82:85], v234, v235 op_sel_hi:[0,0,0]
	v_mfma_scale_f32_16x16x128_f8f6f4 v[78:81], v[2:9], v[216:223], v[78:81], v234, v235 op_sel_hi:[0,0,0]
	v_mfma_scale_f32_16x16x128_f8f6f4 v[74:77], v[10:17], v[216:223], v[74:77], v234, v235 op_sel_hi:[0,0,0]
	v_mfma_scale_f32_16x16x128_f8f6f4 v[70:73], v[2:9], v[224:231], v[70:73], v234, v235 op_sel_hi:[0,0,0]
	v_mfma_scale_f32_16x16x128_f8f6f4 v[66:69], v[10:17], v[224:231], v[66:69], v234, v235 op_sel_hi:[0,0,0]
	v_mfma_scale_f32_16x16x128_f8f6f4 v[62:65], v[2:9], v[244:251], v[62:65], v234, v235 op_sel_hi:[0,0,0]
	v_mfma_scale_f32_16x16x128_f8f6f4 v[58:61], v[10:17], v[244:251], v[58:61], v234, v235 op_sel_hi:[0,0,0]
	s_setprio 0
	s_setprio 1
	v_mfma_scale_f32_16x16x128_f8f6f4 v[54:57], v[26:33], v[206:213], v[54:57], v234, v235 op_sel_hi:[0,0,0]
	v_mfma_scale_f32_16x16x128_f8f6f4 v[50:53], v[198:205], v[206:213], v[50:53], v234, v235 op_sel_hi:[0,0,0]
	v_mfma_scale_f32_16x16x128_f8f6f4 v[46:49], v[26:33], v[216:223], v[46:49], v234, v235 op_sel_hi:[0,0,0]
	v_mfma_scale_f32_16x16x128_f8f6f4 v[42:45], v[198:205], v[216:223], v[42:45], v234, v235 op_sel_hi:[0,0,0]
	v_mfma_scale_f32_16x16x128_f8f6f4 v[38:41], v[26:33], v[224:231], v[38:41], v234, v235 op_sel_hi:[0,0,0]
	v_mfma_scale_f32_16x16x128_f8f6f4 v[34:37], v[198:205], v[224:231], v[34:37], v234, v235 op_sel_hi:[0,0,0]
	v_mfma_scale_f32_16x16x128_f8f6f4 v[154:157], v[26:33], v[244:251], v[154:157], v234, v235 op_sel_hi:[0,0,0]
	v_mfma_scale_f32_16x16x128_f8f6f4 v[158:161], v[198:205], v[244:251], v[158:161], v234, v235 op_sel_hi:[0,0,0]
	s_setprio 0
	s_waitcnt vmcnt(8)
	s_barrier
	ds_read_b128 v[10:13], v184
	ds_read_b128 v[14:17], v185
	ds_read_b128 v[26:29], v186
	ds_read_b128 v[30:33], v187
	ds_read_b128 v[2:5], v188
	ds_read_b128 v[6:9], v189
	ds_read_b128 v[198:201], v190
	ds_read_b128 v[202:205], v191
	v_cndmask_b32_e64 v0, v196, v194, s[4:5]
	v_lshlrev_b32_e32 v170, 10, v0
	s_mov_b32 m0, s10
	v_and_or_b32 v170, v170, s82, v174
	v_bfe_u32 v0, v0, 16, 16
	ds_read_b128 v[206:209], v192 offset:32768
	ds_read_b128 v[210:213], v192 offset:33792
	ds_read_b128 v[216:219], v192 offset:34816
	ds_read_b128 v[220:223], v192 offset:35840
	ds_read_b128 v[224:227], v192 offset:36864
	ds_read_b128 v[228:231], v192 offset:37888
	ds_read_b128 v[244:247], v192 offset:38912
	ds_read_b128 v[248:251], v192 offset:39936
	v_lshl_add_u32 v0, v0, 10, v175
	global_load_lds_dwordx4 v170, s[58:59]
	s_mov_b32 m0, s11
	s_nop 0
	global_load_lds_dwordx4 v0, s[58:59]
	s_waitcnt lgkmcnt(0)
	s_barrier
	s_setprio 1
	s_waitcnt lgkmcnt(0)
	v_mfma_scale_f32_16x16x128_f8f6f4 v[150:153], v[10:17], v[206:213], v[150:153], v234, v235 op_sel_hi:[0,0,0]
	v_mfma_scale_f32_16x16x128_f8f6f4 v[146:149], v[26:33], v[206:213], v[146:149], v234, v235 op_sel_hi:[0,0,0]
	v_mfma_scale_f32_16x16x128_f8f6f4 v[142:145], v[10:17], v[216:223], v[142:145], v234, v235 op_sel_hi:[0,0,0]
	v_mfma_scale_f32_16x16x128_f8f6f4 v[138:141], v[26:33], v[216:223], v[138:141], v234, v235 op_sel_hi:[0,0,0]
	v_mfma_scale_f32_16x16x128_f8f6f4 v[134:137], v[10:17], v[224:231], v[134:137], v234, v235 op_sel_hi:[0,0,0]
	v_mfma_scale_f32_16x16x128_f8f6f4 v[130:133], v[26:33], v[224:231], v[130:133], v234, v235 op_sel_hi:[0,0,0]
	v_mfma_scale_f32_16x16x128_f8f6f4 v[126:129], v[10:17], v[244:251], v[126:129], v234, v235 op_sel_hi:[0,0,0]
	v_mfma_scale_f32_16x16x128_f8f6f4 v[122:125], v[26:33], v[244:251], v[122:125], v234, v235 op_sel_hi:[0,0,0]
	s_setprio 0
	s_setprio 1
	v_mfma_scale_f32_16x16x128_f8f6f4 v[118:121], v[2:9], v[206:213], v[118:121], v234, v235 op_sel_hi:[0,0,0]
	v_mfma_scale_f32_16x16x128_f8f6f4 v[114:117], v[198:205], v[206:213], v[114:117], v234, v235 op_sel_hi:[0,0,0]
	v_mfma_scale_f32_16x16x128_f8f6f4 v[110:113], v[2:9], v[216:223], v[110:113], v234, v235 op_sel_hi:[0,0,0]
	v_mfma_scale_f32_16x16x128_f8f6f4 v[106:109], v[198:205], v[216:223], v[106:109], v234, v235 op_sel_hi:[0,0,0]
	v_mfma_scale_f32_16x16x128_f8f6f4 v[102:105], v[2:9], v[224:231], v[102:105], v234, v235 op_sel_hi:[0,0,0]
	v_mfma_scale_f32_16x16x128_f8f6f4 v[98:101], v[198:205], v[224:231], v[98:101], v234, v235 op_sel_hi:[0,0,0]
	v_mfma_scale_f32_16x16x128_f8f6f4 v[94:97], v[2:9], v[244:251], v[94:97], v234, v235 op_sel_hi:[0,0,0]
	v_mfma_scale_f32_16x16x128_f8f6f4 v[90:93], v[198:205], v[244:251], v[90:93], v234, v235 op_sel_hi:[0,0,0]
	s_setprio 0
	s_waitcnt vmcnt(8)
	s_barrier
	s_mov_b32 m0, s64
	v_lshl_add_u64 v[18:19], v[18:19], 0, s[66:67]
	s_add_u32 s4, s56, 0x20080
	ds_read_b128 v[206:209], v192 offset:49152
	ds_read_b128 v[210:213], v192 offset:50176
	ds_read_b128 v[216:219], v192 offset:51200
	ds_read_b128 v[220:223], v192 offset:52224
	ds_read_b128 v[224:227], v192 offset:53248
	ds_read_b128 v[228:231], v192 offset:54272
	ds_read_b128 v[244:247], v192 offset:55296
	ds_read_b128 v[248:251], v192 offset:56320
	global_load_lds_dwordx4 v[18:19], off
	v_lshl_add_u64 v[18:19], v[20:21], 0, s[66:67]
	s_mov_b32 m0, s81
	s_addc_u32 s5, s57, 0
	global_load_lds_dwordx4 v[18:19], off
	v_lshl_add_u64 v[18:19], s[4:5], 0, v[162:163]
	s_mov_b32 m0, s49
	s_nop 0
	global_load_lds_dwordx4 v[18:19], off
	v_lshl_add_u64 v[18:19], s[4:5], 0, v[164:165]
	s_mov_b32 m0, s30
	s_nop 0
	global_load_lds_dwordx4 v[18:19], off
	v_lshl_add_u64 v[18:19], v[24:25], 0, s[66:67]
	s_mov_b32 m0, s6
	s_nop 0
	global_load_lds_dwordx4 v[18:19], off
	v_lshl_add_u64 v[18:19], v[22:23], 0, s[66:67]
	s_mov_b32 m0, s7
	s_nop 0
	global_load_lds_dwordx4 v[18:19], off
	s_waitcnt lgkmcnt(0)
	s_barrier
	s_setprio 1
	s_waitcnt lgkmcnt(0)
	v_mfma_scale_f32_16x16x128_f8f6f4 v[86:89], v[10:17], v[206:213], v[86:89], v234, v235 op_sel_hi:[0,0,0]
	v_mfma_scale_f32_16x16x128_f8f6f4 v[82:85], v[26:33], v[206:213], v[82:85], v234, v235 op_sel_hi:[0,0,0]
	v_mfma_scale_f32_16x16x128_f8f6f4 v[78:81], v[10:17], v[216:223], v[78:81], v234, v235 op_sel_hi:[0,0,0]
	v_mfma_scale_f32_16x16x128_f8f6f4 v[74:77], v[26:33], v[216:223], v[74:77], v234, v235 op_sel_hi:[0,0,0]
	v_mfma_scale_f32_16x16x128_f8f6f4 v[70:73], v[10:17], v[224:231], v[70:73], v234, v235 op_sel_hi:[0,0,0]
	v_mfma_scale_f32_16x16x128_f8f6f4 v[66:69], v[26:33], v[224:231], v[66:69], v234, v235 op_sel_hi:[0,0,0]
	v_mfma_scale_f32_16x16x128_f8f6f4 v[62:65], v[10:17], v[244:251], v[62:65], v234, v235 op_sel_hi:[0,0,0]
	v_mfma_scale_f32_16x16x128_f8f6f4 v[58:61], v[26:33], v[244:251], v[58:61], v234, v235 op_sel_hi:[0,0,0]
	s_setprio 0
	s_setprio 1
	v_mfma_scale_f32_16x16x128_f8f6f4 v[54:57], v[2:9], v[206:213], v[54:57], v234, v235 op_sel_hi:[0,0,0]
	v_mfma_scale_f32_16x16x128_f8f6f4 v[50:53], v[198:205], v[206:213], v[50:53], v234, v235 op_sel_hi:[0,0,0]
	v_mfma_scale_f32_16x16x128_f8f6f4 v[46:49], v[2:9], v[216:223], v[46:49], v234, v235 op_sel_hi:[0,0,0]
	v_mfma_scale_f32_16x16x128_f8f6f4 v[42:45], v[198:205], v[216:223], v[42:45], v234, v235 op_sel_hi:[0,0,0]
	v_mfma_scale_f32_16x16x128_f8f6f4 v[38:41], v[2:9], v[224:231], v[38:41], v234, v235 op_sel_hi:[0,0,0]
	v_mfma_scale_f32_16x16x128_f8f6f4 v[34:37], v[198:205], v[224:231], v[34:37], v234, v235 op_sel_hi:[0,0,0]
	v_mfma_scale_f32_16x16x128_f8f6f4 v[154:157], v[2:9], v[244:251], v[154:157], v234, v235 op_sel_hi:[0,0,0]
	v_mfma_scale_f32_16x16x128_f8f6f4 v[158:161], v[198:205], v[244:251], v[158:161], v234, v235 op_sel_hi:[0,0,0]
	s_setprio 0
	s_waitcnt vmcnt(8)
	s_barrier
	s_add_i32 s74, s74, 2
	s_add_u32 s54, s54, 0x100
	s_addc_u32 s55, s55, 0
	s_add_u32 s43, s43, 0x100
	s_addc_u32 s45, s45, 0
	s_cmp_gt_u32 s74, 5
	s_cbranch_scc1 .LBB0_2005
